# attention fast path v2: fully coalesced Q/K/Vt loads (8 lanes per row + DPP reductions), LDS p-table instead of readlane broadcast
# speedup vs baseline: 1.1398x; 1.0842x over previous
_Z8attn_fwdPKDF16_S0_S0_PKjPf:
	s_mov_b64 s[36:37], s[0:1]
	s_mov_b32 s38, s2
	s_load_dwordx4 s[8:11], s[0:1], 0x0
	s_load_dwordx4 s[12:15], s[0:1], 0x10
	s_load_dwordx2 s[16:17], s[0:1], 0x20
	s_lshl_b32 s3, s2, 1
	s_mul_hi_u32 s4, s2, 0xaaaaaaab
	s_and_b32 s3, s3, 14
	s_lshr_b32 s4, s4, 6
	s_add_i32 s6, s3, s4
	s_lshr_b32 s5, s2, 3
	s_mul_hi_u32 s7, s5, 0x15555556
	s_mul_i32 s7, s7, 12
	s_sub_i32 s20, s5, s7
	v_and_b32_e32 v1, 63, v0
	v_readfirstlane_b32 s19, v0
	v_and_b32_e32 v2, 3, v1
	v_lshrrev_b32_e32 v3, 2, v1
	s_lshr_b32 s19, s19, 6
	s_lshl_b32 s18, s19, 5
	s_lshl_b32 s26, s19, 12
	v_lshl_add_u32 v4, v1, 4, s26
	v_mul_u32_u24_e32 v5, 0x1800, v3
	v_lshl_add_u32 v5, v2, 4, v5
	v_add_u32_e32 v6, 0x18000, v5
	v_add_u32_e32 v7, 0x30000, v5
	v_add_u32_e32 v8, 0x48000, v5
	v_min_u32_e32 v9, 47, v1
	v_lshlrev_b32_e32 v9, 2, v9
	s_mul_i32 s21, s6, 0xc00
	s_cmp_lt_u32 s20, 11
	s_cselect_b32 s22, 1, 0
	s_cselect_b32 s40, 0, 0xf149f2ca
	s_add_i32 s22, s20, s22
	s_cmp_gt_u32 s20, 0
	s_cselect_b32 s23, 1, 0
	s_cselect_b32 s41, 0, 0xf149f2ca
	s_sub_i32 s23, s20, s23
	s_cmp_lt_u32 s20, 10
	s_cselect_b32 s24, 2, 0
	s_cselect_b32 s42, 0, 0xf149f2ca
	s_add_i32 s24, s20, s24
	s_cmp_gt_u32 s20, 1
	s_cselect_b32 s25, 2, 0
	s_cselect_b32 s43, 0, 0xf149f2ca
	s_sub_i32 s25, s20, s25
	s_waitcnt lgkmcnt(0)
	s_lshl_b32 s26, s20, 8
	s_add_i32 s26, s26, s21
	s_lshl_b32 s26, s26, 7
	s_add_u32 s44, s10, s26
	s_addc_u32 s45, s11, 0
	s_add_u32 s54, s8, s26
	s_addc_u32 s55, s9, 0
	s_lshl_b32 s27, s20, 8
	s_add_i32 s27, s27, s21
	s_add_i32 s27, s27, s18
	s_lshl_b32 s27, s27, 8
	s_add_u32 s62, s16, s27
	s_addc_u32 s63, s17, 0
	s_lshl_b32 s26, s22, 8
	s_add_i32 s26, s26, s21
	s_lshl_b32 s26, s26, 7
	s_add_u32 s46, s10, s26
	s_addc_u32 s47, s11, 0
	s_lshl_b32 s26, s23, 8
	s_add_i32 s26, s26, s21
	s_lshl_b32 s26, s26, 7
	s_add_u32 s48, s10, s26
	s_addc_u32 s49, s11, 0
	s_lshl_b32 s26, s24, 8
	s_add_i32 s26, s26, s21
	s_lshl_b32 s26, s26, 7
	s_add_u32 s50, s10, s26
	s_addc_u32 s51, s11, 0
	s_lshl_b32 s26, s25, 8
	s_add_i32 s26, s26, s21
	s_lshl_b32 s26, s26, 7
	s_add_u32 s52, s10, s26
	s_addc_u32 s53, s11, 0
	s_mul_i32 s28, s6, 0x30000
	s_add_i32 s28, s28, s18
	s_lshl_b32 s26, s20, 8
	s_add_i32 s26, s26, s28
	s_lshl_b32 s26, s26, 1
	s_add_u32 s56, s12, s26
	s_addc_u32 s57, s13, 0
	s_lshl_b32 s26, s22, 8
	s_add_i32 s26, s26, s28
	s_lshl_b32 s26, s26, 1
	s_add_u32 s58, s12, s26
	s_addc_u32 s59, s13, 0
	s_lshl_b32 s26, s23, 8
	s_add_i32 s26, s26, s28
	s_lshl_b32 s26, s26, 1
	s_add_u32 s60, s12, s26
	s_addc_u32 s61, s13, 0
	s_mul_i32 s26, s6, 0xc0
	s_add_u32 s64, s14, s26
	s_addc_u32 s65, s15, 0
	global_load_dword v10, v9, s[64:65]
	global_load_dwordx4 v[96:99], v4, s[54:55] nt
	global_load_dwordx4 v[100:103], v4, s[54:55] offset:1024 nt
	global_load_dwordx4 v[104:107], v4, s[54:55] offset:2048 nt
	global_load_dwordx4 v[108:111], v4, s[54:55] offset:3072 nt
	global_load_dwordx4 v[112:115], v4, s[44:45]
	global_load_dwordx4 v[116:119], v4, s[44:45] offset:1024
	global_load_dwordx4 v[120:123], v4, s[44:45] offset:2048
	global_load_dwordx4 v[124:127], v4, s[44:45] offset:3072
	global_load_dwordx4 v[128:131], v4, s[46:47]
	global_load_dwordx4 v[132:135], v4, s[46:47] offset:1024
	global_load_dwordx4 v[136:139], v4, s[46:47] offset:2048
	global_load_dwordx4 v[140:143], v4, s[46:47] offset:3072
	global_load_dwordx4 v[144:147], v4, s[48:49]
	global_load_dwordx4 v[148:151], v4, s[48:49] offset:1024
	global_load_dwordx4 v[152:155], v4, s[48:49] offset:2048
	global_load_dwordx4 v[156:159], v4, s[48:49] offset:3072
	global_load_dwordx4 v[160:163], v4, s[50:51]
	global_load_dwordx4 v[164:167], v4, s[50:51] offset:1024
	global_load_dwordx4 v[168:171], v4, s[50:51] offset:2048
	global_load_dwordx4 v[172:175], v4, s[50:51] offset:3072
	global_load_dwordx4 v[176:179], v4, s[52:53]
	global_load_dwordx4 v[180:183], v4, s[52:53] offset:1024
	global_load_dwordx4 v[184:187], v4, s[52:53] offset:2048
	global_load_dwordx4 v[188:191], v4, s[52:53] offset:3072
	global_load_dwordx4 v[192:195], v5, s[56:57]
	global_load_dwordx4 v[196:199], v6, s[56:57]
	global_load_dwordx4 v[200:203], v7, s[56:57]
	global_load_dwordx4 v[204:207], v8, s[56:57]
	global_load_dwordx4 v[208:211], v5, s[58:59]
	global_load_dwordx4 v[212:215], v6, s[58:59]
	global_load_dwordx4 v[216:219], v7, s[58:59]
	global_load_dwordx4 v[220:223], v8, s[58:59]
	global_load_dwordx4 v[224:227], v5, s[60:61]
	global_load_dwordx4 v[228:231], v6, s[60:61]
	global_load_dwordx4 v[232:235], v7, s[60:61]
	global_load_dwordx4 v[236:239], v8, s[60:61]
	s_waitcnt vmcnt(32)
	v_max_f32_dpp v11, v10, v10 quad_perm:[1,0,3,2] row_mask:0xf bank_mask:0xf
	v_fma_mix_f32 v64, v96, v96, 0 op_sel_hi:[1,1,0]
	v_fma_mix_f32 v65, v100, v100, 0 op_sel_hi:[1,1,0]
	v_fma_mix_f32 v66, v104, v104, 0 op_sel_hi:[1,1,0]
	v_fma_mix_f32 v67, v108, v108, 0 op_sel_hi:[1,1,0]
	v_max_f32_dpp v11, v11, v11 quad_perm:[2,3,0,1] row_mask:0xf bank_mask:0xf
	v_fma_mix_f32 v64, v96, v96, v64 op_sel:[1,1,0] op_sel_hi:[1,1,0]
	v_fma_mix_f32 v65, v100, v100, v65 op_sel:[1,1,0] op_sel_hi:[1,1,0]
	v_fma_mix_f32 v66, v104, v104, v66 op_sel:[1,1,0] op_sel_hi:[1,1,0]
	v_fma_mix_f32 v67, v108, v108, v67 op_sel:[1,1,0] op_sel_hi:[1,1,0]
	v_max_f32_dpp v11, v11, v11 row_half_mirror row_mask:0xf bank_mask:0xf
	v_fma_mix_f32 v64, v97, v97, v64 op_sel_hi:[1,1,0]
	v_fma_mix_f32 v65, v101, v101, v65 op_sel_hi:[1,1,0]
	v_fma_mix_f32 v66, v105, v105, v66 op_sel_hi:[1,1,0]
	v_fma_mix_f32 v67, v109, v109, v67 op_sel_hi:[1,1,0]
	v_max_f32_dpp v11, v11, v11 row_mirror row_mask:0xf bank_mask:0xf
	v_fma_mix_f32 v64, v97, v97, v64 op_sel:[1,1,0] op_sel_hi:[1,1,0]
	v_fma_mix_f32 v65, v101, v101, v65 op_sel:[1,1,0] op_sel_hi:[1,1,0]
	v_fma_mix_f32 v66, v105, v105, v66 op_sel:[1,1,0] op_sel_hi:[1,1,0]
	v_fma_mix_f32 v67, v109, v109, v67 op_sel:[1,1,0] op_sel_hi:[1,1,0]
	v_fma_mix_f32 v64, v98, v98, v64 op_sel_hi:[1,1,0]
	v_fma_mix_f32 v65, v102, v102, v65 op_sel_hi:[1,1,0]
	v_fma_mix_f32 v66, v106, v106, v66 op_sel_hi:[1,1,0]
	v_fma_mix_f32 v67, v110, v110, v67 op_sel_hi:[1,1,0]
	v_fma_mix_f32 v64, v98, v98, v64 op_sel:[1,1,0] op_sel_hi:[1,1,0]
	v_fma_mix_f32 v65, v102, v102, v65 op_sel:[1,1,0] op_sel_hi:[1,1,0]
	v_fma_mix_f32 v66, v106, v106, v66 op_sel:[1,1,0] op_sel_hi:[1,1,0]
	v_fma_mix_f32 v67, v110, v110, v67 op_sel:[1,1,0] op_sel_hi:[1,1,0]
	v_fma_mix_f32 v64, v99, v99, v64 op_sel_hi:[1,1,0]
	v_fma_mix_f32 v65, v103, v103, v65 op_sel_hi:[1,1,0]
	v_fma_mix_f32 v66, v107, v107, v66 op_sel_hi:[1,1,0]
	v_fma_mix_f32 v67, v111, v111, v67 op_sel_hi:[1,1,0]
	v_fma_mix_f32 v64, v99, v99, v64 op_sel:[1,1,0] op_sel_hi:[1,1,0]
	v_fma_mix_f32 v65, v103, v103, v65 op_sel:[1,1,0] op_sel_hi:[1,1,0]
	v_fma_mix_f32 v66, v107, v107, v66 op_sel:[1,1,0] op_sel_hi:[1,1,0]
	v_fma_mix_f32 v67, v111, v111, v67 op_sel:[1,1,0] op_sel_hi:[1,1,0]
	v_add_f32_dpp v64, v64, v64 quad_perm:[1,0,3,2] row_mask:0xf bank_mask:0xf
	v_add_f32_dpp v65, v65, v65 quad_perm:[1,0,3,2] row_mask:0xf bank_mask:0xf
	v_add_f32_dpp v66, v66, v66 quad_perm:[1,0,3,2] row_mask:0xf bank_mask:0xf
	v_add_f32_dpp v67, v67, v67 quad_perm:[1,0,3,2] row_mask:0xf bank_mask:0xf
	v_add_f32_dpp v64, v64, v64 quad_perm:[2,3,0,1] row_mask:0xf bank_mask:0xf
	v_add_f32_dpp v65, v65, v65 quad_perm:[2,3,0,1] row_mask:0xf bank_mask:0xf
	v_add_f32_dpp v66, v66, v66 quad_perm:[2,3,0,1] row_mask:0xf bank_mask:0xf
	v_add_f32_dpp v67, v67, v67 quad_perm:[2,3,0,1] row_mask:0xf bank_mask:0xf
	v_add_f32_dpp v64, v64, v64 row_half_mirror row_mask:0xf bank_mask:0xf
	v_add_f32_dpp v65, v65, v65 row_half_mirror row_mask:0xf bank_mask:0xf
	v_add_f32_dpp v66, v66, v66 row_half_mirror row_mask:0xf bank_mask:0xf
	v_add_f32_dpp v67, v67, v67 row_half_mirror row_mask:0xf bank_mask:0xf
	v_max3_f32 v68, v64, v65, v66
	v_readlane_b32 s26, v11, 0
	v_max_f32_e32 v68, v68, v67
	v_readlane_b32 s27, v11, 16
	v_readlane_b32 s28, v11, 32
	v_max_f32_dpp v68, v68, v68 row_mirror row_mask:0xf bank_mask:0xf
	v_readlane_b32 s29, v11, 48
	v_mov_b32_e32 v69, s26
	v_max_f32_e32 v69, s27, v69
	v_max_f32_e32 v69, s28, v69
	v_max_f32_e32 v69, s29, v69
	v_readlane_b32 s26, v68, 0
	v_readlane_b32 s27, v68, 16
	v_readlane_b32 s28, v68, 32
	v_readlane_b32 s29, v68, 48
	v_sqrt_f32_e32 v69, v69
	v_mov_b32_e32 v70, s26
	v_max_f32_e32 v70, s27, v70
	v_max_f32_e32 v70, s28, v70
	v_max_f32_e32 v70, s29, v70
	v_mul_f32_e32 v69, 0x3f8020c5, v69
	v_sqrt_f32_e32 v70, v70
	s_nop 0
	v_mul_f32_e32 v70, 0x3f8020c5, v70
	v_mul_f32_e32 v69, v69, v70
	v_add_f32_e32 v69, 0x42191384, v69
	s_waitcnt vmcnt(12)
	v_fma_mix_f32 v12, v96, v112, 0 op_sel_hi:[1,1,0]
	v_fma_mix_f32 v13, v100, v116, 0 op_sel_hi:[1,1,0]
	v_fma_mix_f32 v14, v104, v120, 0 op_sel_hi:[1,1,0]
	v_fma_mix_f32 v15, v108, v124, 0 op_sel_hi:[1,1,0]
	v_fma_mix_f32 v16, v96, v128, 0 op_sel_hi:[1,1,0]
	v_fma_mix_f32 v17, v100, v132, 0 op_sel_hi:[1,1,0]
	v_fma_mix_f32 v18, v104, v136, 0 op_sel_hi:[1,1,0]
	v_fma_mix_f32 v19, v108, v140, 0 op_sel_hi:[1,1,0]
	v_fma_mix_f32 v20, v96, v144, 0 op_sel_hi:[1,1,0]
	v_fma_mix_f32 v21, v100, v148, 0 op_sel_hi:[1,1,0]
	v_fma_mix_f32 v22, v104, v152, 0 op_sel_hi:[1,1,0]
	v_fma_mix_f32 v23, v108, v156, 0 op_sel_hi:[1,1,0]
	v_fma_mix_f32 v24, v96, v160, 0 op_sel_hi:[1,1,0]
	v_fma_mix_f32 v25, v100, v164, 0 op_sel_hi:[1,1,0]
	v_fma_mix_f32 v26, v104, v168, 0 op_sel_hi:[1,1,0]
	v_fma_mix_f32 v27, v108, v172, 0 op_sel_hi:[1,1,0]
	v_fma_mix_f32 v28, v96, v176, 0 op_sel_hi:[1,1,0]
	v_fma_mix_f32 v29, v100, v180, 0 op_sel_hi:[1,1,0]
	v_fma_mix_f32 v30, v104, v184, 0 op_sel_hi:[1,1,0]
	v_fma_mix_f32 v31, v108, v188, 0 op_sel_hi:[1,1,0]
	v_fma_mix_f32 v12, v96, v112, v12 op_sel:[1,1,0] op_sel_hi:[1,1,0]
	v_fma_mix_f32 v13, v100, v116, v13 op_sel:[1,1,0] op_sel_hi:[1,1,0]
	v_fma_mix_f32 v14, v104, v120, v14 op_sel:[1,1,0] op_sel_hi:[1,1,0]
	v_fma_mix_f32 v15, v108, v124, v15 op_sel:[1,1,0] op_sel_hi:[1,1,0]
	v_fma_mix_f32 v16, v96, v128, v16 op_sel:[1,1,0] op_sel_hi:[1,1,0]
	v_fma_mix_f32 v17, v100, v132, v17 op_sel:[1,1,0] op_sel_hi:[1,1,0]
	v_fma_mix_f32 v18, v104, v136, v18 op_sel:[1,1,0] op_sel_hi:[1,1,0]
	v_fma_mix_f32 v19, v108, v140, v19 op_sel:[1,1,0] op_sel_hi:[1,1,0]
	v_fma_mix_f32 v20, v96, v144, v20 op_sel:[1,1,0] op_sel_hi:[1,1,0]
	v_fma_mix_f32 v21, v100, v148, v21 op_sel:[1,1,0] op_sel_hi:[1,1,0]
	v_fma_mix_f32 v22, v104, v152, v22 op_sel:[1,1,0] op_sel_hi:[1,1,0]
	v_fma_mix_f32 v23, v108, v156, v23 op_sel:[1,1,0] op_sel_hi:[1,1,0]
	v_fma_mix_f32 v24, v96, v160, v24 op_sel:[1,1,0] op_sel_hi:[1,1,0]
	v_fma_mix_f32 v25, v100, v164, v25 op_sel:[1,1,0] op_sel_hi:[1,1,0]
	v_fma_mix_f32 v26, v104, v168, v26 op_sel:[1,1,0] op_sel_hi:[1,1,0]
	v_fma_mix_f32 v27, v108, v172, v27 op_sel:[1,1,0] op_sel_hi:[1,1,0]
	v_fma_mix_f32 v28, v96, v176, v28 op_sel:[1,1,0] op_sel_hi:[1,1,0]
	v_fma_mix_f32 v29, v100, v180, v29 op_sel:[1,1,0] op_sel_hi:[1,1,0]
	v_fma_mix_f32 v30, v104, v184, v30 op_sel:[1,1,0] op_sel_hi:[1,1,0]
	v_fma_mix_f32 v31, v108, v188, v31 op_sel:[1,1,0] op_sel_hi:[1,1,0]
	v_fma_mix_f32 v12, v97, v113, v12 op_sel_hi:[1,1,0]
	v_fma_mix_f32 v13, v101, v117, v13 op_sel_hi:[1,1,0]
	v_fma_mix_f32 v14, v105, v121, v14 op_sel_hi:[1,1,0]
	v_fma_mix_f32 v15, v109, v125, v15 op_sel_hi:[1,1,0]
	v_fma_mix_f32 v16, v97, v129, v16 op_sel_hi:[1,1,0]
	v_fma_mix_f32 v17, v101, v133, v17 op_sel_hi:[1,1,0]
	v_fma_mix_f32 v18, v105, v137, v18 op_sel_hi:[1,1,0]
	v_fma_mix_f32 v19, v109, v141, v19 op_sel_hi:[1,1,0]
	v_fma_mix_f32 v20, v97, v145, v20 op_sel_hi:[1,1,0]
	v_fma_mix_f32 v21, v101, v149, v21 op_sel_hi:[1,1,0]
	v_fma_mix_f32 v22, v105, v153, v22 op_sel_hi:[1,1,0]
	v_fma_mix_f32 v23, v109, v157, v23 op_sel_hi:[1,1,0]
	v_fma_mix_f32 v24, v97, v161, v24 op_sel_hi:[1,1,0]
	v_fma_mix_f32 v25, v101, v165, v25 op_sel_hi:[1,1,0]
	v_fma_mix_f32 v26, v105, v169, v26 op_sel_hi:[1,1,0]
	v_fma_mix_f32 v27, v109, v173, v27 op_sel_hi:[1,1,0]
	v_fma_mix_f32 v28, v97, v177, v28 op_sel_hi:[1,1,0]
	v_fma_mix_f32 v29, v101, v181, v29 op_sel_hi:[1,1,0]
	v_fma_mix_f32 v30, v105, v185, v30 op_sel_hi:[1,1,0]
	v_fma_mix_f32 v31, v109, v189, v31 op_sel_hi:[1,1,0]
	v_fma_mix_f32 v12, v97, v113, v12 op_sel:[1,1,0] op_sel_hi:[1,1,0]
	v_fma_mix_f32 v13, v101, v117, v13 op_sel:[1,1,0] op_sel_hi:[1,1,0]
	v_fma_mix_f32 v14, v105, v121, v14 op_sel:[1,1,0] op_sel_hi:[1,1,0]
	v_fma_mix_f32 v15, v109, v125, v15 op_sel:[1,1,0] op_sel_hi:[1,1,0]
	v_fma_mix_f32 v16, v97, v129, v16 op_sel:[1,1,0] op_sel_hi:[1,1,0]
	v_fma_mix_f32 v17, v101, v133, v17 op_sel:[1,1,0] op_sel_hi:[1,1,0]
	v_fma_mix_f32 v18, v105, v137, v18 op_sel:[1,1,0] op_sel_hi:[1,1,0]
	v_fma_mix_f32 v19, v109, v141, v19 op_sel:[1,1,0] op_sel_hi:[1,1,0]
	v_fma_mix_f32 v20, v97, v145, v20 op_sel:[1,1,0] op_sel_hi:[1,1,0]
	v_fma_mix_f32 v21, v101, v149, v21 op_sel:[1,1,0] op_sel_hi:[1,1,0]
	v_fma_mix_f32 v22, v105, v153, v22 op_sel:[1,1,0] op_sel_hi:[1,1,0]
	v_fma_mix_f32 v23, v109, v157, v23 op_sel:[1,1,0] op_sel_hi:[1,1,0]
	v_fma_mix_f32 v24, v97, v161, v24 op_sel:[1,1,0] op_sel_hi:[1,1,0]
	v_fma_mix_f32 v25, v101, v165, v25 op_sel:[1,1,0] op_sel_hi:[1,1,0]
	v_fma_mix_f32 v26, v105, v169, v26 op_sel:[1,1,0] op_sel_hi:[1,1,0]
	v_fma_mix_f32 v27, v109, v173, v27 op_sel:[1,1,0] op_sel_hi:[1,1,0]
	v_fma_mix_f32 v28, v97, v177, v28 op_sel:[1,1,0] op_sel_hi:[1,1,0]
	v_fma_mix_f32 v29, v101, v181, v29 op_sel:[1,1,0] op_sel_hi:[1,1,0]
	v_fma_mix_f32 v30, v105, v185, v30 op_sel:[1,1,0] op_sel_hi:[1,1,0]
	v_fma_mix_f32 v31, v109, v189, v31 op_sel:[1,1,0] op_sel_hi:[1,1,0]
	v_fma_mix_f32 v12, v98, v114, v12 op_sel_hi:[1,1,0]
	v_fma_mix_f32 v13, v102, v118, v13 op_sel_hi:[1,1,0]
	v_fma_mix_f32 v14, v106, v122, v14 op_sel_hi:[1,1,0]
	v_fma_mix_f32 v15, v110, v126, v15 op_sel_hi:[1,1,0]
	v_fma_mix_f32 v16, v98, v130, v16 op_sel_hi:[1,1,0]
	v_fma_mix_f32 v17, v102, v134, v17 op_sel_hi:[1,1,0]
	v_fma_mix_f32 v18, v106, v138, v18 op_sel_hi:[1,1,0]
	v_fma_mix_f32 v19, v110, v142, v19 op_sel_hi:[1,1,0]
	v_fma_mix_f32 v20, v98, v146, v20 op_sel_hi:[1,1,0]
	v_fma_mix_f32 v21, v102, v150, v21 op_sel_hi:[1,1,0]
	v_fma_mix_f32 v22, v106, v154, v22 op_sel_hi:[1,1,0]
	v_fma_mix_f32 v23, v110, v158, v23 op_sel_hi:[1,1,0]
	v_fma_mix_f32 v24, v98, v162, v24 op_sel_hi:[1,1,0]
	v_fma_mix_f32 v25, v102, v166, v25 op_sel_hi:[1,1,0]
	v_fma_mix_f32 v26, v106, v170, v26 op_sel_hi:[1,1,0]
	v_fma_mix_f32 v27, v110, v174, v27 op_sel_hi:[1,1,0]
	v_fma_mix_f32 v28, v98, v178, v28 op_sel_hi:[1,1,0]
	v_fma_mix_f32 v29, v102, v182, v29 op_sel_hi:[1,1,0]
	v_fma_mix_f32 v30, v106, v186, v30 op_sel_hi:[1,1,0]
	v_fma_mix_f32 v31, v110, v190, v31 op_sel_hi:[1,1,0]
	v_fma_mix_f32 v12, v98, v114, v12 op_sel:[1,1,0] op_sel_hi:[1,1,0]
	v_fma_mix_f32 v13, v102, v118, v13 op_sel:[1,1,0] op_sel_hi:[1,1,0]
	v_fma_mix_f32 v14, v106, v122, v14 op_sel:[1,1,0] op_sel_hi:[1,1,0]
	v_fma_mix_f32 v15, v110, v126, v15 op_sel:[1,1,0] op_sel_hi:[1,1,0]
	v_fma_mix_f32 v16, v98, v130, v16 op_sel:[1,1,0] op_sel_hi:[1,1,0]
	v_fma_mix_f32 v17, v102, v134, v17 op_sel:[1,1,0] op_sel_hi:[1,1,0]
	v_fma_mix_f32 v18, v106, v138, v18 op_sel:[1,1,0] op_sel_hi:[1,1,0]
	v_fma_mix_f32 v19, v110, v142, v19 op_sel:[1,1,0] op_sel_hi:[1,1,0]
	v_fma_mix_f32 v20, v98, v146, v20 op_sel:[1,1,0] op_sel_hi:[1,1,0]
	v_fma_mix_f32 v21, v102, v150, v21 op_sel:[1,1,0] op_sel_hi:[1,1,0]
	v_fma_mix_f32 v22, v106, v154, v22 op_sel:[1,1,0] op_sel_hi:[1,1,0]
	v_fma_mix_f32 v23, v110, v158, v23 op_sel:[1,1,0] op_sel_hi:[1,1,0]
	v_fma_mix_f32 v24, v98, v162, v24 op_sel:[1,1,0] op_sel_hi:[1,1,0]
	v_fma_mix_f32 v25, v102, v166, v25 op_sel:[1,1,0] op_sel_hi:[1,1,0]
	v_fma_mix_f32 v26, v106, v170, v26 op_sel:[1,1,0] op_sel_hi:[1,1,0]
	v_fma_mix_f32 v27, v110, v174, v27 op_sel:[1,1,0] op_sel_hi:[1,1,0]
	v_fma_mix_f32 v28, v98, v178, v28 op_sel:[1,1,0] op_sel_hi:[1,1,0]
	v_fma_mix_f32 v29, v102, v182, v29 op_sel:[1,1,0] op_sel_hi:[1,1,0]
	v_fma_mix_f32 v30, v106, v186, v30 op_sel:[1,1,0] op_sel_hi:[1,1,0]
	v_fma_mix_f32 v31, v110, v190, v31 op_sel:[1,1,0] op_sel_hi:[1,1,0]
	v_fma_mix_f32 v12, v99, v115, v12 op_sel_hi:[1,1,0]
	v_fma_mix_f32 v13, v103, v119, v13 op_sel_hi:[1,1,0]
	v_fma_mix_f32 v14, v107, v123, v14 op_sel_hi:[1,1,0]
	v_fma_mix_f32 v15, v111, v127, v15 op_sel_hi:[1,1,0]
	v_fma_mix_f32 v16, v99, v131, v16 op_sel_hi:[1,1,0]
	v_fma_mix_f32 v17, v103, v135, v17 op_sel_hi:[1,1,0]
	v_fma_mix_f32 v18, v107, v139, v18 op_sel_hi:[1,1,0]
	v_fma_mix_f32 v19, v111, v143, v19 op_sel_hi:[1,1,0]
	v_fma_mix_f32 v20, v99, v147, v20 op_sel_hi:[1,1,0]
	v_fma_mix_f32 v21, v103, v151, v21 op_sel_hi:[1,1,0]
	v_fma_mix_f32 v22, v107, v155, v22 op_sel_hi:[1,1,0]
	v_fma_mix_f32 v23, v111, v159, v23 op_sel_hi:[1,1,0]
	v_fma_mix_f32 v24, v99, v163, v24 op_sel_hi:[1,1,0]
	v_fma_mix_f32 v25, v103, v167, v25 op_sel_hi:[1,1,0]
	v_fma_mix_f32 v26, v107, v171, v26 op_sel_hi:[1,1,0]
	v_fma_mix_f32 v27, v111, v175, v27 op_sel_hi:[1,1,0]
	v_fma_mix_f32 v28, v99, v179, v28 op_sel_hi:[1,1,0]
	v_fma_mix_f32 v29, v103, v183, v29 op_sel_hi:[1,1,0]
	v_fma_mix_f32 v30, v107, v187, v30 op_sel_hi:[1,1,0]
	v_fma_mix_f32 v31, v111, v191, v31 op_sel_hi:[1,1,0]
	v_fma_mix_f32 v12, v99, v115, v12 op_sel:[1,1,0] op_sel_hi:[1,1,0]
	v_fma_mix_f32 v13, v103, v119, v13 op_sel:[1,1,0] op_sel_hi:[1,1,0]
	v_fma_mix_f32 v14, v107, v123, v14 op_sel:[1,1,0] op_sel_hi:[1,1,0]
	v_fma_mix_f32 v15, v111, v127, v15 op_sel:[1,1,0] op_sel_hi:[1,1,0]
	v_fma_mix_f32 v16, v99, v131, v16 op_sel:[1,1,0] op_sel_hi:[1,1,0]
	v_fma_mix_f32 v17, v103, v135, v17 op_sel:[1,1,0] op_sel_hi:[1,1,0]
	v_fma_mix_f32 v18, v107, v139, v18 op_sel:[1,1,0] op_sel_hi:[1,1,0]
	v_fma_mix_f32 v19, v111, v143, v19 op_sel:[1,1,0] op_sel_hi:[1,1,0]
	v_fma_mix_f32 v20, v99, v147, v20 op_sel:[1,1,0] op_sel_hi:[1,1,0]
	v_fma_mix_f32 v21, v103, v151, v21 op_sel:[1,1,0] op_sel_hi:[1,1,0]
	v_fma_mix_f32 v22, v107, v155, v22 op_sel:[1,1,0] op_sel_hi:[1,1,0]
	v_fma_mix_f32 v23, v111, v159, v23 op_sel:[1,1,0] op_sel_hi:[1,1,0]
	v_fma_mix_f32 v24, v99, v163, v24 op_sel:[1,1,0] op_sel_hi:[1,1,0]
	v_fma_mix_f32 v25, v103, v167, v25 op_sel:[1,1,0] op_sel_hi:[1,1,0]
	v_fma_mix_f32 v26, v107, v171, v26 op_sel:[1,1,0] op_sel_hi:[1,1,0]
	v_fma_mix_f32 v27, v111, v175, v27 op_sel:[1,1,0] op_sel_hi:[1,1,0]
	v_fma_mix_f32 v28, v99, v179, v28 op_sel:[1,1,0] op_sel_hi:[1,1,0]
	v_fma_mix_f32 v29, v103, v183, v29 op_sel:[1,1,0] op_sel_hi:[1,1,0]
	v_fma_mix_f32 v30, v107, v187, v30 op_sel:[1,1,0] op_sel_hi:[1,1,0]
	v_fma_mix_f32 v31, v111, v191, v31 op_sel:[1,1,0] op_sel_hi:[1,1,0]
	v_add_f32_dpp v12, v12, v12 quad_perm:[1,0,3,2] row_mask:0xf bank_mask:0xf
	v_add_f32_dpp v13, v13, v13 quad_perm:[1,0,3,2] row_mask:0xf bank_mask:0xf
	v_add_f32_dpp v14, v14, v14 quad_perm:[1,0,3,2] row_mask:0xf bank_mask:0xf
	v_add_f32_dpp v15, v15, v15 quad_perm:[1,0,3,2] row_mask:0xf bank_mask:0xf
	v_add_f32_dpp v16, v16, v16 quad_perm:[1,0,3,2] row_mask:0xf bank_mask:0xf
	v_add_f32_dpp v17, v17, v17 quad_perm:[1,0,3,2] row_mask:0xf bank_mask:0xf
	v_add_f32_dpp v18, v18, v18 quad_perm:[1,0,3,2] row_mask:0xf bank_mask:0xf
	v_add_f32_dpp v19, v19, v19 quad_perm:[1,0,3,2] row_mask:0xf bank_mask:0xf
	v_add_f32_dpp v20, v20, v20 quad_perm:[1,0,3,2] row_mask:0xf bank_mask:0xf
	v_add_f32_dpp v21, v21, v21 quad_perm:[1,0,3,2] row_mask:0xf bank_mask:0xf
	v_add_f32_dpp v22, v22, v22 quad_perm:[1,0,3,2] row_mask:0xf bank_mask:0xf
	v_add_f32_dpp v23, v23, v23 quad_perm:[1,0,3,2] row_mask:0xf bank_mask:0xf
	v_add_f32_dpp v24, v24, v24 quad_perm:[1,0,3,2] row_mask:0xf bank_mask:0xf
	v_add_f32_dpp v25, v25, v25 quad_perm:[1,0,3,2] row_mask:0xf bank_mask:0xf
	v_add_f32_dpp v26, v26, v26 quad_perm:[1,0,3,2] row_mask:0xf bank_mask:0xf
	v_add_f32_dpp v27, v27, v27 quad_perm:[1,0,3,2] row_mask:0xf bank_mask:0xf
	v_add_f32_dpp v28, v28, v28 quad_perm:[1,0,3,2] row_mask:0xf bank_mask:0xf
	v_add_f32_dpp v29, v29, v29 quad_perm:[1,0,3,2] row_mask:0xf bank_mask:0xf
	v_add_f32_dpp v30, v30, v30 quad_perm:[1,0,3,2] row_mask:0xf bank_mask:0xf
	v_add_f32_dpp v31, v31, v31 quad_perm:[1,0,3,2] row_mask:0xf bank_mask:0xf
	v_add_f32_dpp v12, v12, v12 quad_perm:[2,3,0,1] row_mask:0xf bank_mask:0xf
	v_add_f32_dpp v13, v13, v13 quad_perm:[2,3,0,1] row_mask:0xf bank_mask:0xf
	v_add_f32_dpp v14, v14, v14 quad_perm:[2,3,0,1] row_mask:0xf bank_mask:0xf
	v_add_f32_dpp v15, v15, v15 quad_perm:[2,3,0,1] row_mask:0xf bank_mask:0xf
	v_add_f32_dpp v16, v16, v16 quad_perm:[2,3,0,1] row_mask:0xf bank_mask:0xf
	v_add_f32_dpp v17, v17, v17 quad_perm:[2,3,0,1] row_mask:0xf bank_mask:0xf
	v_add_f32_dpp v18, v18, v18 quad_perm:[2,3,0,1] row_mask:0xf bank_mask:0xf
	v_add_f32_dpp v19, v19, v19 quad_perm:[2,3,0,1] row_mask:0xf bank_mask:0xf
	v_add_f32_dpp v20, v20, v20 quad_perm:[2,3,0,1] row_mask:0xf bank_mask:0xf
	v_add_f32_dpp v21, v21, v21 quad_perm:[2,3,0,1] row_mask:0xf bank_mask:0xf
	v_add_f32_dpp v22, v22, v22 quad_perm:[2,3,0,1] row_mask:0xf bank_mask:0xf
	v_add_f32_dpp v23, v23, v23 quad_perm:[2,3,0,1] row_mask:0xf bank_mask:0xf
	v_add_f32_dpp v24, v24, v24 quad_perm:[2,3,0,1] row_mask:0xf bank_mask:0xf
	v_add_f32_dpp v25, v25, v25 quad_perm:[2,3,0,1] row_mask:0xf bank_mask:0xf
	v_add_f32_dpp v26, v26, v26 quad_perm:[2,3,0,1] row_mask:0xf bank_mask:0xf
	v_add_f32_dpp v27, v27, v27 quad_perm:[2,3,0,1] row_mask:0xf bank_mask:0xf
	v_add_f32_dpp v28, v28, v28 quad_perm:[2,3,0,1] row_mask:0xf bank_mask:0xf
	v_add_f32_dpp v29, v29, v29 quad_perm:[2,3,0,1] row_mask:0xf bank_mask:0xf
	v_add_f32_dpp v30, v30, v30 quad_perm:[2,3,0,1] row_mask:0xf bank_mask:0xf
	v_add_f32_dpp v31, v31, v31 quad_perm:[2,3,0,1] row_mask:0xf bank_mask:0xf
	v_add_f32_dpp v12, v12, v12 row_half_mirror row_mask:0xf bank_mask:0xf
	v_add_f32_dpp v13, v13, v13 row_half_mirror row_mask:0xf bank_mask:0xf
	v_add_f32_dpp v14, v14, v14 row_half_mirror row_mask:0xf bank_mask:0xf
	v_add_f32_dpp v15, v15, v15 row_half_mirror row_mask:0xf bank_mask:0xf
	v_add_f32_dpp v16, v16, v16 row_half_mirror row_mask:0xf bank_mask:0xf
	v_add_f32_dpp v17, v17, v17 row_half_mirror row_mask:0xf bank_mask:0xf
	v_add_f32_dpp v18, v18, v18 row_half_mirror row_mask:0xf bank_mask:0xf
	v_add_f32_dpp v19, v19, v19 row_half_mirror row_mask:0xf bank_mask:0xf
	v_add_f32_dpp v20, v20, v20 row_half_mirror row_mask:0xf bank_mask:0xf
	v_add_f32_dpp v21, v21, v21 row_half_mirror row_mask:0xf bank_mask:0xf
	v_add_f32_dpp v22, v22, v22 row_half_mirror row_mask:0xf bank_mask:0xf
	v_add_f32_dpp v23, v23, v23 row_half_mirror row_mask:0xf bank_mask:0xf
	v_add_f32_dpp v24, v24, v24 row_half_mirror row_mask:0xf bank_mask:0xf
	v_add_f32_dpp v25, v25, v25 row_half_mirror row_mask:0xf bank_mask:0xf
	v_add_f32_dpp v26, v26, v26 row_half_mirror row_mask:0xf bank_mask:0xf
	v_add_f32_dpp v27, v27, v27 row_half_mirror row_mask:0xf bank_mask:0xf
	v_add_f32_dpp v28, v28, v28 row_half_mirror row_mask:0xf bank_mask:0xf
	v_add_f32_dpp v29, v29, v29 row_half_mirror row_mask:0xf bank_mask:0xf
	v_add_f32_dpp v30, v30, v30 row_half_mirror row_mask:0xf bank_mask:0xf
	v_add_f32_dpp v31, v31, v31 row_half_mirror row_mask:0xf bank_mask:0xf
	v_add_f32_e32 v12, 0x42e59caf, v12
	v_add_f32_e32 v13, 0x42e59caf, v13
	v_add_f32_e32 v14, 0x42e59caf, v14
	v_add_f32_e32 v15, 0x42e59caf, v15
	v_add_f32_e32 v16, 0x42e59caf, v16
	v_add_f32_e32 v17, 0x42e59caf, v17
	v_add_f32_e32 v18, 0x42e59caf, v18
	v_add_f32_e32 v19, 0x42e59caf, v19
	v_add_f32_e32 v20, 0x42e59caf, v20
	v_add_f32_e32 v21, 0x42e59caf, v21
	v_add_f32_e32 v22, 0x42e59caf, v22
	v_add_f32_e32 v23, 0x42e59caf, v23
	v_add_f32_e32 v24, 0x42659caf, v24
	v_add_f32_e32 v25, 0x42659caf, v25
	v_add_f32_e32 v26, 0x42659caf, v26
	v_add_f32_e32 v27, 0x42659caf, v27
	v_add_f32_e32 v28, 0x42659caf, v28
	v_add_f32_e32 v29, 0x42659caf, v29
	v_add_f32_e32 v30, 0x42659caf, v30
	v_add_f32_e32 v31, 0x42659caf, v31
	v_add_f32_e32 v16, s40, v16
	v_add_f32_e32 v17, s40, v17
	v_add_f32_e32 v18, s40, v18
	v_add_f32_e32 v19, s40, v19
	v_add_f32_e32 v20, s41, v20
	v_add_f32_e32 v21, s41, v21
	v_add_f32_e32 v22, s41, v22
	v_add_f32_e32 v23, s41, v23
	v_add_f32_e32 v24, s42, v24
	v_add_f32_e32 v25, s42, v25
	v_add_f32_e32 v26, s42, v26
	v_add_f32_e32 v27, s42, v27
	v_add_f32_e32 v28, s43, v28
	v_add_f32_e32 v29, s43, v29
	v_add_f32_e32 v30, s43, v30
	v_add_f32_e32 v31, s43, v31
	v_max3_f32 v112, v12, v16, v20
	v_max3_f32 v113, v13, v17, v21
	v_max3_f32 v114, v14, v18, v22
	v_max3_f32 v115, v15, v19, v23
	v_sub_f32_e32 v116, v12, v112
	v_sub_f32_e32 v117, v13, v113
	v_sub_f32_e32 v118, v14, v114
	v_sub_f32_e32 v119, v15, v115
	v_sub_f32_e32 v120, v16, v112
	v_sub_f32_e32 v121, v17, v113
	v_sub_f32_e32 v122, v18, v114
	v_sub_f32_e32 v123, v19, v115
	v_sub_f32_e32 v124, v20, v112
	v_sub_f32_e32 v125, v21, v113
	v_sub_f32_e32 v126, v22, v114
	v_sub_f32_e32 v127, v23, v115
	v_exp_f32_e32 v116, v116
	v_exp_f32_e32 v117, v117
	v_exp_f32_e32 v118, v118
	v_exp_f32_e32 v119, v119
	v_exp_f32_e32 v120, v120
	v_exp_f32_e32 v121, v121
	v_exp_f32_e32 v122, v122
	v_exp_f32_e32 v123, v123
	v_exp_f32_e32 v124, v124
	v_exp_f32_e32 v125, v125
	v_exp_f32_e32 v126, v126
	v_exp_f32_e32 v127, v127
	v_max_f32_e32 v132, v24, v28
	v_max_f32_e32 v133, v25, v29
	v_max_f32_e32 v134, v26, v30
	v_max_f32_e32 v135, v27, v31
	v_sub_f32_e32 v132, v132, v112
	v_sub_f32_e32 v133, v133, v113
	v_sub_f32_e32 v134, v134, v114
	v_sub_f32_e32 v135, v135, v115
	v_max3_f32 v136, v132, v133, v134
	v_min3_f32 v137, v112, v113, v114
	v_max_f32_e32 v136, v136, v135
	v_min_f32_e32 v137, v137, v115
	v_add_f32_e32 v128, v116, v120
	v_add_f32_e32 v129, v117, v121
	v_add_f32_e32 v130, v118, v122
	v_add_f32_e32 v131, v119, v123
	v_min_f32_dpp v137, v137, v137 row_mirror row_mask:0xf bank_mask:0xf
	v_add_f32_e32 v128, v128, v124
	v_add_f32_e32 v129, v129, v125
	v_add_f32_e32 v130, v130, v126
	v_add_f32_e32 v131, v131, v127
	s_mov_b32 s30, 0xc2200a3d
	v_cmp_ngt_f32_e32 vcc, s30, v136
	s_cmp_lg_u64 vcc, 0
	s_cselect_b32 s31, 1, 0
	v_readlane_b32 s26, v137, 0
	v_readlane_b32 s27, v137, 16
	v_readlane_b32 s28, v137, 32
	v_readlane_b32 s29, v137, 48
	s_nop 1
	v_mov_b32_e32 v138, s26
	v_min_f32_e32 v138, s27, v138
	v_min_f32_e32 v138, s28, v138
	v_min_f32_e32 v138, s29, v138
	v_sub_f32_e32 v69, v69, v138
	v_cmp_ngt_f32_e32 vcc, s30, v69
	s_cmp_lg_u64 vcc, 0
	s_cselect_b32 s26, 1, 0
	s_or_b32 s31, s31, s26
	s_lshl_b32 s26, s19, 2
	s_add_i32 s26, s26, 0x20700
	v_mov_b32_e32 v139, s26
	v_mov_b32_e32 v140, s31
	ds_write_b32 v139, v140
	v_div_scale_f32 v141, s[26:27], v128, v128, 1.0
	v_rcp_f32_e32 v142, v141
	s_nop 0
	v_fma_f32 v143, -v141, v142, 1.0
	v_fmac_f32_e32 v142, v143, v142
	v_div_scale_f32 v143, vcc, 1.0, v128, 1.0
	v_mul_f32_e32 v144, v143, v142
	v_fma_f32 v145, -v141, v144, v143
	v_fmac_f32_e32 v144, v145, v142
	v_fma_f32 v141, -v141, v144, v143
	v_div_fmas_f32 v141, v141, v142, v144
	v_div_fixup_f32 v128, v141, v128, 1.0
	v_div_scale_f32 v141, s[26:27], v129, v129, 1.0
	v_rcp_f32_e32 v142, v141
	s_nop 0
	v_fma_f32 v143, -v141, v142, 1.0
	v_fmac_f32_e32 v142, v143, v142
	v_div_scale_f32 v143, vcc, 1.0, v129, 1.0
	v_mul_f32_e32 v144, v143, v142
	v_fma_f32 v145, -v141, v144, v143
	v_fmac_f32_e32 v144, v145, v142
	v_fma_f32 v141, -v141, v144, v143
	v_div_fmas_f32 v141, v141, v142, v144
	v_div_fixup_f32 v129, v141, v129, 1.0
	v_div_scale_f32 v141, s[26:27], v130, v130, 1.0
	v_rcp_f32_e32 v142, v141
	s_nop 0
	v_fma_f32 v143, -v141, v142, 1.0
	v_fmac_f32_e32 v142, v143, v142
	v_div_scale_f32 v143, vcc, 1.0, v130, 1.0
	v_mul_f32_e32 v144, v143, v142
	v_fma_f32 v145, -v141, v144, v143
	v_fmac_f32_e32 v144, v145, v142
	v_fma_f32 v141, -v141, v144, v143
	v_div_fmas_f32 v141, v141, v142, v144
	v_div_fixup_f32 v130, v141, v130, 1.0
	v_div_scale_f32 v141, s[26:27], v131, v131, 1.0
	v_rcp_f32_e32 v142, v141
	s_nop 0
	v_fma_f32 v143, -v141, v142, 1.0
	v_fmac_f32_e32 v142, v143, v142
	v_div_scale_f32 v143, vcc, 1.0, v131, 1.0
	v_mul_f32_e32 v144, v143, v142
	v_fma_f32 v145, -v141, v144, v143
	v_fmac_f32_e32 v144, v145, v142
	v_fma_f32 v141, -v141, v144, v143
	v_div_fmas_f32 v141, v141, v142, v144
	v_div_fixup_f32 v131, v141, v131, 1.0
	v_mul_f32_e32 v116, v116, v128
	v_mul_f32_e32 v117, v117, v129
	v_mul_f32_e32 v118, v118, v130
	v_mul_f32_e32 v119, v119, v131
	v_mul_f32_e32 v120, v120, v128
	v_mul_f32_e32 v121, v121, v129
	v_mul_f32_e32 v122, v122, v130
	v_mul_f32_e32 v123, v123, v131
	v_mul_f32_e32 v124, v124, v128
	v_mul_f32_e32 v125, v125, v129
	v_mul_f32_e32 v126, v126, v130
	v_mul_f32_e32 v127, v127, v131
	s_waitcnt lgkmcnt(0)
	s_barrier
	v_mov_b32_e32 v139, 0x20700
	ds_read_b128 v[144:147], v139
	ds_read_b128 v[148:151], v139 offset:16
	v_lshrrev_b32_e32 v152, 3, v1
	v_and_b32_e32 v153, 3, v152
	v_lshrrev_b32_e32 v152, 2, v152
	v_lshlrev_b32_e32 v152, 5, v152
	v_lshl_or_b32 v152, v153, 2, v152
	s_lshl_b32 s26, s19, 9
	s_add_i32 s26, s26, 0x18000
	v_add_u32_e32 v152, s26, v152
	v_lshl_add_u32 v153, v2, 5, s26
	s_waitcnt lgkmcnt(0)
	v_or3_b32 v144, v144, v145, v146
	v_or3_b32 v148, v148, v149, v150
	v_or3_b32 v144, v144, v147, v148
	v_or_b32_e32 v144, v144, v151
	s_nop 0
	v_readfirstlane_b32 s27, v144
	s_nop 3
	s_cmp_lg_u32 s27, 0
	s_cbranch_scc1 .Lattn_fallback
	ds_write_b32 v152, v116
	ds_write_b32 v152, v117 offset:16
	ds_write_b32 v152, v118 offset:64
	ds_write_b32 v152, v119 offset:80
	ds_write_b32 v152, v120 offset:128
	ds_write_b32 v152, v121 offset:144
	ds_write_b32 v152, v122 offset:192
	ds_write_b32 v152, v123 offset:208
	ds_write_b32 v152, v124 offset:256
	ds_write_b32 v152, v125 offset:272
	ds_write_b32 v152, v126 offset:320
	ds_write_b32 v152, v127 offset:336
	ds_read_b128 v[64:67], v153
	ds_read_b128 v[68:71], v153 offset:16
	ds_read_b128 v[72:75], v153 offset:128
	ds_read_b128 v[76:79], v153 offset:144
	ds_read_b128 v[80:83], v153 offset:256
	ds_read_b128 v[84:87], v153 offset:272
	v_lshrrev_b32_e32 v154, 1, v2
	v_and_b32_e32 v155, 1, v2
	v_lshlrev_b32_e32 v154, 4, v154
	v_lshl_or_b32 v154, v155, 2, v154
	v_mul_u32_u24_e32 v154, 0x110, v154
	v_lshl_add_u32 v154, v3, 2, v154
	s_mul_i32 s26, s19, 0x2200
	v_add_u32_e32 v154, s26, v154
	s_waitcnt vmcnt(0) lgkmcnt(0)
	v_fma_mix_f32 v32, v192, v64, 0 op_sel:[0,0,0] op_sel_hi:[1,0,0]
	v_fma_mix_f32 v33, v192, v65, 0 op_sel:[1,0,0] op_sel_hi:[1,0,0]
	v_fma_mix_f32 v34, v193, v66, 0 op_sel:[0,0,0] op_sel_hi:[1,0,0]
	v_fma_mix_f32 v35, v193, v67, 0 op_sel:[1,0,0] op_sel_hi:[1,0,0]
	v_fma_mix_f32 v36, v194, v68, 0 op_sel:[0,0,0] op_sel_hi:[1,0,0]
	v_fma_mix_f32 v37, v194, v69, 0 op_sel:[1,0,0] op_sel_hi:[1,0,0]
	v_fma_mix_f32 v38, v195, v70, 0 op_sel:[0,0,0] op_sel_hi:[1,0,0]
	v_fma_mix_f32 v39, v195, v71, 0 op_sel:[1,0,0] op_sel_hi:[1,0,0]
	v_fma_mix_f32 v40, v196, v64, 0 op_sel:[0,0,0] op_sel_hi:[1,0,0]
	v_fma_mix_f32 v41, v196, v65, 0 op_sel:[1,0,0] op_sel_hi:[1,0,0]
	v_fma_mix_f32 v42, v197, v66, 0 op_sel:[0,0,0] op_sel_hi:[1,0,0]
	v_fma_mix_f32 v43, v197, v67, 0 op_sel:[1,0,0] op_sel_hi:[1,0,0]
	v_fma_mix_f32 v44, v198, v68, 0 op_sel:[0,0,0] op_sel_hi:[1,0,0]
	v_fma_mix_f32 v45, v198, v69, 0 op_sel:[1,0,0] op_sel_hi:[1,0,0]
	v_fma_mix_f32 v46, v199, v70, 0 op_sel:[0,0,0] op_sel_hi:[1,0,0]
	v_fma_mix_f32 v47, v199, v71, 0 op_sel:[1,0,0] op_sel_hi:[1,0,0]
	v_fma_mix_f32 v48, v200, v64, 0 op_sel:[0,0,0] op_sel_hi:[1,0,0]
	v_fma_mix_f32 v49, v200, v65, 0 op_sel:[1,0,0] op_sel_hi:[1,0,0]
	v_fma_mix_f32 v50, v201, v66, 0 op_sel:[0,0,0] op_sel_hi:[1,0,0]
	v_fma_mix_f32 v51, v201, v67, 0 op_sel:[1,0,0] op_sel_hi:[1,0,0]
	v_fma_mix_f32 v52, v202, v68, 0 op_sel:[0,0,0] op_sel_hi:[1,0,0]
	v_fma_mix_f32 v53, v202, v69, 0 op_sel:[1,0,0] op_sel_hi:[1,0,0]
	v_fma_mix_f32 v54, v203, v70, 0 op_sel:[0,0,0] op_sel_hi:[1,0,0]
	v_fma_mix_f32 v55, v203, v71, 0 op_sel:[1,0,0] op_sel_hi:[1,0,0]
	v_fma_mix_f32 v56, v204, v64, 0 op_sel:[0,0,0] op_sel_hi:[1,0,0]
	v_fma_mix_f32 v57, v204, v65, 0 op_sel:[1,0,0] op_sel_hi:[1,0,0]
	v_fma_mix_f32 v58, v205, v66, 0 op_sel:[0,0,0] op_sel_hi:[1,0,0]
	v_fma_mix_f32 v59, v205, v67, 0 op_sel:[1,0,0] op_sel_hi:[1,0,0]
	v_fma_mix_f32 v60, v206, v68, 0 op_sel:[0,0,0] op_sel_hi:[1,0,0]
	v_fma_mix_f32 v61, v206, v69, 0 op_sel:[1,0,0] op_sel_hi:[1,0,0]
	v_fma_mix_f32 v62, v207, v70, 0 op_sel:[0,0,0] op_sel_hi:[1,0,0]
	v_fma_mix_f32 v63, v207, v71, 0 op_sel:[1,0,0] op_sel_hi:[1,0,0]
	v_fma_mix_f32 v32, v208, v72, v32 op_sel:[0,0,0] op_sel_hi:[1,0,0]
	v_fma_mix_f32 v33, v208, v73, v33 op_sel:[1,0,0] op_sel_hi:[1,0,0]
	v_fma_mix_f32 v34, v209, v74, v34 op_sel:[0,0,0] op_sel_hi:[1,0,0]
	v_fma_mix_f32 v35, v209, v75, v35 op_sel:[1,0,0] op_sel_hi:[1,0,0]
	v_fma_mix_f32 v36, v210, v76, v36 op_sel:[0,0,0] op_sel_hi:[1,0,0]
	v_fma_mix_f32 v37, v210, v77, v37 op_sel:[1,0,0] op_sel_hi:[1,0,0]
	v_fma_mix_f32 v38, v211, v78, v38 op_sel:[0,0,0] op_sel_hi:[1,0,0]
	v_fma_mix_f32 v39, v211, v79, v39 op_sel:[1,0,0] op_sel_hi:[1,0,0]
	v_fma_mix_f32 v40, v212, v72, v40 op_sel:[0,0,0] op_sel_hi:[1,0,0]
	v_fma_mix_f32 v41, v212, v73, v41 op_sel:[1,0,0] op_sel_hi:[1,0,0]
	v_fma_mix_f32 v42, v213, v74, v42 op_sel:[0,0,0] op_sel_hi:[1,0,0]
	v_fma_mix_f32 v43, v213, v75, v43 op_sel:[1,0,0] op_sel_hi:[1,0,0]
	v_fma_mix_f32 v44, v214, v76, v44 op_sel:[0,0,0] op_sel_hi:[1,0,0]
	v_fma_mix_f32 v45, v214, v77, v45 op_sel:[1,0,0] op_sel_hi:[1,0,0]
	v_fma_mix_f32 v46, v215, v78, v46 op_sel:[0,0,0] op_sel_hi:[1,0,0]
	v_fma_mix_f32 v47, v215, v79, v47 op_sel:[1,0,0] op_sel_hi:[1,0,0]
	v_fma_mix_f32 v48, v216, v72, v48 op_sel:[0,0,0] op_sel_hi:[1,0,0]
	v_fma_mix_f32 v49, v216, v73, v49 op_sel:[1,0,0] op_sel_hi:[1,0,0]
	v_fma_mix_f32 v50, v217, v74, v50 op_sel:[0,0,0] op_sel_hi:[1,0,0]
	v_fma_mix_f32 v51, v217, v75, v51 op_sel:[1,0,0] op_sel_hi:[1,0,0]
	v_fma_mix_f32 v52, v218, v76, v52 op_sel:[0,0,0] op_sel_hi:[1,0,0]
	v_fma_mix_f32 v53, v218, v77, v53 op_sel:[1,0,0] op_sel_hi:[1,0,0]
	v_fma_mix_f32 v54, v219, v78, v54 op_sel:[0,0,0] op_sel_hi:[1,0,0]
	v_fma_mix_f32 v55, v219, v79, v55 op_sel:[1,0,0] op_sel_hi:[1,0,0]
	v_fma_mix_f32 v56, v220, v72, v56 op_sel:[0,0,0] op_sel_hi:[1,0,0]
	v_fma_mix_f32 v57, v220, v73, v57 op_sel:[1,0,0] op_sel_hi:[1,0,0]
	v_fma_mix_f32 v58, v221, v74, v58 op_sel:[0,0,0] op_sel_hi:[1,0,0]
	v_fma_mix_f32 v59, v221, v75, v59 op_sel:[1,0,0] op_sel_hi:[1,0,0]
	v_fma_mix_f32 v60, v222, v76, v60 op_sel:[0,0,0] op_sel_hi:[1,0,0]
	v_fma_mix_f32 v61, v222, v77, v61 op_sel:[1,0,0] op_sel_hi:[1,0,0]
	v_fma_mix_f32 v62, v223, v78, v62 op_sel:[0,0,0] op_sel_hi:[1,0,0]
	v_fma_mix_f32 v63, v223, v79, v63 op_sel:[1,0,0] op_sel_hi:[1,0,0]
	v_fma_mix_f32 v32, v224, v80, v32 op_sel:[0,0,0] op_sel_hi:[1,0,0]
	v_fma_mix_f32 v33, v224, v81, v33 op_sel:[1,0,0] op_sel_hi:[1,0,0]
	v_fma_mix_f32 v34, v225, v82, v34 op_sel:[0,0,0] op_sel_hi:[1,0,0]
	v_fma_mix_f32 v35, v225, v83, v35 op_sel:[1,0,0] op_sel_hi:[1,0,0]
	v_fma_mix_f32 v36, v226, v84, v36 op_sel:[0,0,0] op_sel_hi:[1,0,0]
	v_fma_mix_f32 v37, v226, v85, v37 op_sel:[1,0,0] op_sel_hi:[1,0,0]
	v_fma_mix_f32 v38, v227, v86, v38 op_sel:[0,0,0] op_sel_hi:[1,0,0]
	v_fma_mix_f32 v39, v227, v87, v39 op_sel:[1,0,0] op_sel_hi:[1,0,0]
	v_fma_mix_f32 v40, v228, v80, v40 op_sel:[0,0,0] op_sel_hi:[1,0,0]
	v_fma_mix_f32 v41, v228, v81, v41 op_sel:[1,0,0] op_sel_hi:[1,0,0]
	v_fma_mix_f32 v42, v229, v82, v42 op_sel:[0,0,0] op_sel_hi:[1,0,0]
	v_fma_mix_f32 v43, v229, v83, v43 op_sel:[1,0,0] op_sel_hi:[1,0,0]
	v_fma_mix_f32 v44, v230, v84, v44 op_sel:[0,0,0] op_sel_hi:[1,0,0]
	v_fma_mix_f32 v45, v230, v85, v45 op_sel:[1,0,0] op_sel_hi:[1,0,0]
	v_fma_mix_f32 v46, v231, v86, v46 op_sel:[0,0,0] op_sel_hi:[1,0,0]
	v_fma_mix_f32 v47, v231, v87, v47 op_sel:[1,0,0] op_sel_hi:[1,0,0]
	v_fma_mix_f32 v48, v232, v80, v48 op_sel:[0,0,0] op_sel_hi:[1,0,0]
	v_fma_mix_f32 v49, v232, v81, v49 op_sel:[1,0,0] op_sel_hi:[1,0,0]
	v_fma_mix_f32 v50, v233, v82, v50 op_sel:[0,0,0] op_sel_hi:[1,0,0]
	v_fma_mix_f32 v51, v233, v83, v51 op_sel:[1,0,0] op_sel_hi:[1,0,0]
	v_fma_mix_f32 v52, v234, v84, v52 op_sel:[0,0,0] op_sel_hi:[1,0,0]
	v_fma_mix_f32 v53, v234, v85, v53 op_sel:[1,0,0] op_sel_hi:[1,0,0]
	v_fma_mix_f32 v54, v235, v86, v54 op_sel:[0,0,0] op_sel_hi:[1,0,0]
	v_fma_mix_f32 v55, v235, v87, v55 op_sel:[1,0,0] op_sel_hi:[1,0,0]
	v_fma_mix_f32 v56, v236, v80, v56 op_sel:[0,0,0] op_sel_hi:[1,0,0]
	v_fma_mix_f32 v57, v236, v81, v57 op_sel:[1,0,0] op_sel_hi:[1,0,0]
	v_fma_mix_f32 v58, v237, v82, v58 op_sel:[0,0,0] op_sel_hi:[1,0,0]
	v_fma_mix_f32 v59, v237, v83, v59 op_sel:[1,0,0] op_sel_hi:[1,0,0]
	v_fma_mix_f32 v60, v238, v84, v60 op_sel:[0,0,0] op_sel_hi:[1,0,0]
	v_fma_mix_f32 v61, v238, v85, v61 op_sel:[1,0,0] op_sel_hi:[1,0,0]
	v_fma_mix_f32 v62, v239, v86, v62 op_sel:[0,0,0] op_sel_hi:[1,0,0]
	v_fma_mix_f32 v63, v239, v87, v63 op_sel:[1,0,0] op_sel_hi:[1,0,0]
	ds_write_b32 v154, v32
	ds_write_b32 v154, v33 offset:272
	ds_write_b32 v154, v34 offset:544
	ds_write_b32 v154, v35 offset:816
	ds_write_b32 v154, v36 offset:2176
	ds_write_b32 v154, v37 offset:2448
	ds_write_b32 v154, v38 offset:2720
	ds_write_b32 v154, v39 offset:2992
	ds_write_b32 v154, v40 offset:64
	ds_write_b32 v154, v41 offset:336
	ds_write_b32 v154, v42 offset:608
	ds_write_b32 v154, v43 offset:880
	ds_write_b32 v154, v44 offset:2240
	ds_write_b32 v154, v45 offset:2512
	ds_write_b32 v154, v46 offset:2784
	ds_write_b32 v154, v47 offset:3056
	ds_write_b32 v154, v48 offset:128
	ds_write_b32 v154, v49 offset:400
	ds_write_b32 v154, v50 offset:672
	ds_write_b32 v154, v51 offset:944
	ds_write_b32 v154, v52 offset:2304
	ds_write_b32 v154, v53 offset:2576
	ds_write_b32 v154, v54 offset:2848
	ds_write_b32 v154, v55 offset:3120
	ds_write_b32 v154, v56 offset:192
	ds_write_b32 v154, v57 offset:464
	ds_write_b32 v154, v58 offset:736
	ds_write_b32 v154, v59 offset:1008
	ds_write_b32 v154, v60 offset:2368
	ds_write_b32 v154, v61 offset:2640
	ds_write_b32 v154, v62 offset:2912
	ds_write_b32 v154, v63 offset:3184
	v_lshrrev_b32_e32 v81, 4, v1
	v_and_b32_e32 v82, 15, v1
	v_mul_u32_u24_e32 v83, 0x110, v81
	v_lshl_add_u32 v83, v82, 4, v83
	v_add_u32_e32 v83, s26, v83
	v_lshlrev_b32_e32 v84, 8, v81
	v_lshl_add_u32 v84, v82, 4, v84
	v_add_u32_e32 v85, 0x1000, v84
	ds_read_b128 v[32:35], v83
	ds_read_b128 v[36:39], v83 offset:1088
	ds_read_b128 v[40:43], v83 offset:2176
	ds_read_b128 v[44:47], v83 offset:3264
	ds_read_b128 v[48:51], v83 offset:4352
	ds_read_b128 v[52:55], v83 offset:5440
	ds_read_b128 v[56:59], v83 offset:6528
	ds_read_b128 v[60:63], v83 offset:7616
	s_waitcnt lgkmcnt(7)
	global_store_dwordx4 v84, v[32:35], s[62:63] sc1
	s_waitcnt lgkmcnt(6)
	global_store_dwordx4 v84, v[36:39], s[62:63] offset:1024 sc1
	s_waitcnt lgkmcnt(5)
	global_store_dwordx4 v84, v[40:43], s[62:63] offset:2048 sc1
	s_waitcnt lgkmcnt(4)
	global_store_dwordx4 v84, v[44:47], s[62:63] offset:3072 sc1
	s_waitcnt lgkmcnt(3)
	global_store_dwordx4 v85, v[48:51], s[62:63] sc1
	s_waitcnt lgkmcnt(2)
	global_store_dwordx4 v85, v[52:55], s[62:63] offset:1024 sc1
	s_waitcnt lgkmcnt(1)
	global_store_dwordx4 v85, v[56:59], s[62:63] offset:2048 sc1
	s_waitcnt lgkmcnt(0)
	global_store_dwordx4 v85, v[60:63], s[62:63] offset:3072 sc1
	s_endpgm
